# v53 + router phase: token x row and gain row fetched once (16 loads, one round trip) and kept in registers for all three passes; inner loops unrolled
# speedup vs baseline: 1.0051x; 1.0051x over previous
.LBB6_1829:
	v_ashrrev_i32_e32 v13, 31, v12
	v_readlane_b32 s0, v254, 4
	v_lshlrev_b64 v[4:5], 13, v[12:13]
	v_readlane_b32 s1, v254, 5
	v_readlane_b32 s6, v254, 33
	v_readlane_b32 s7, v254, 34
	v_lshl_add_u64 v[4:5], s[0:1], 0, v[4:5]
	v_lshl_add_u64 v[8:9], v[4:5], 0, v[2:3]
	global_load_dwordx4 v[88:91], v[8:9], off
	global_load_dwordx4 v[92:95], v[8:9], off offset:1024
	global_load_dwordx4 v[96:99], v[8:9], off offset:2048
	global_load_dwordx4 v[100:103], v[8:9], off offset:3072
	v_add_co_u32_e32 v84, vcc, 0x1000, v8
	s_nop 1
	v_addc_co_u32_e32 v85, vcc, 0, v9, vcc
	global_load_dwordx4 v[104:107], v[84:85], off
	global_load_dwordx4 v[108:111], v[84:85], off offset:1024
	global_load_dwordx4 v[112:115], v[84:85], off offset:2048
	global_load_dwordx4 v[116:119], v[84:85], off offset:3072
	v_add_co_u32_e32 v86, vcc, 0x2000, v22
	s_nop 1
	v_addc_co_u32_e32 v87, vcc, 0, v23, vcc
	global_load_dwordx4 v[120:123], v[86:87], off
	global_load_dwordx4 v[124:127], v[86:87], off offset:1024
	global_load_dwordx4 v[128:131], v[86:87], off offset:2048
	global_load_dwordx4 v[132:135], v[86:87], off offset:3072
	v_add_co_u32_e32 v86, vcc, 0x1000, v86
	s_nop 1
	v_addc_co_u32_e32 v87, vcc, 0, v87, vcc
	global_load_dwordx4 v[136:139], v[86:87], off
	global_load_dwordx4 v[140:143], v[86:87], off offset:1024
	global_load_dwordx4 v[144:147], v[86:87], off offset:2048
	global_load_dwordx4 v[148:151], v[86:87], off offset:3072
	s_waitcnt vmcnt(8)
	v_mov_b64_e32 v[4:5], v[88:89]
	v_mov_b64_e32 v[6:7], v[90:91]
	v_add_co_u32_e32 v26, vcc, s45, v8
	s_mov_b64 s[8:9], 0
	s_nop 0
	v_addc_co_u32_e32 v27, vcc, 0, v9, vcc
	v_mul_f32_e32 v10, v5, v5
	v_fmac_f32_e32 v10, v4, v4
	v_fmac_f32_e32 v10, v6, v6
	v_fmac_f32_e32 v10, v7, v7
	v_mov_b64_e32 v[4:5], v[92:93]
	v_mov_b64_e32 v[6:7], v[94:95]
	v_mul_f32_e32 v5, v5, v5
	v_fmac_f32_e32 v5, v4, v4
	v_fmac_f32_e32 v5, v6, v6
	v_fmac_f32_e32 v5, v7, v7
	v_add_f32_e32 v10, v10, v5
	v_mov_b64_e32 v[4:5], v[96:97]
	v_mov_b64_e32 v[6:7], v[98:99]
	v_mul_f32_e32 v5, v5, v5
	v_fmac_f32_e32 v5, v4, v4
	v_fmac_f32_e32 v5, v6, v6
	v_fmac_f32_e32 v5, v7, v7
	v_add_f32_e32 v10, v10, v5
	v_mov_b64_e32 v[4:5], v[100:101]
	v_mov_b64_e32 v[6:7], v[102:103]
	v_mul_f32_e32 v5, v5, v5
	v_fmac_f32_e32 v5, v4, v4
	v_fmac_f32_e32 v5, v6, v6
	v_fmac_f32_e32 v5, v7, v7
	v_add_f32_e32 v30, v10, v5
	v_mov_b64_e32 v[4:5], v[104:105]
	v_mov_b64_e32 v[6:7], v[106:107]
	v_mov_b64_e32 v[8:9], v[108:109]
	v_mov_b64_e32 v[10:11], v[110:111]
	v_mov_b32_e32 v28, v4
	v_mov_b32_e32 v29, v8
	v_mov_b32_e32 v8, v5
	v_pk_mul_f32 v[4:5], v[8:9], v[8:9]
	v_mov_b32_e32 v8, v6
	v_pk_fma_f32 v[4:5], v[28:29], v[28:29], v[4:5]
	v_mov_b32_e32 v9, v10
	v_pk_fma_f32 v[4:5], v[8:9], v[8:9], v[4:5]
	v_mov_b32_e32 v10, v7
	v_pk_fma_f32 v[4:5], v[10:11], v[10:11], v[4:5]
	s_nop 0
	v_add_f32_e32 v4, v30, v4
	v_add_f32_e32 v28, v4, v5
	v_mov_b64_e32 v[4:5], v[112:113]
	v_mov_b64_e32 v[6:7], v[114:115]
	v_mov_b64_e32 v[8:9], v[116:117]
	v_mov_b64_e32 v[10:11], v[118:119]
	v_mov_b32_e32 v26, v4
	v_mov_b32_e32 v27, v8
	v_mov_b32_e32 v8, v5
	v_pk_mul_f32 v[4:5], v[8:9], v[8:9]
	v_mov_b32_e32 v8, v6
	v_pk_fma_f32 v[4:5], v[26:27], v[26:27], v[4:5]
	v_mov_b32_e32 v9, v10
	v_pk_fma_f32 v[4:5], v[8:9], v[8:9], v[4:5]
	v_mov_b32_e32 v10, v7
	v_pk_fma_f32 v[4:5], v[10:11], v[10:11], v[4:5]
	s_nop 0
	v_add_f32_e32 v4, v28, v4
	v_add_f32_e32 v4, v4, v5
	ds_bpermute_b32 v5, v25, v4
	v_mov_b64_e32 v[28:29], v[20:21]
	s_waitcnt lgkmcnt(0)
	v_add_f32_e32 v4, v4, v5
	ds_bpermute_b32 v5, v40, v4
	s_waitcnt lgkmcnt(0)
	v_add_f32_e32 v4, v4, v5
	ds_bpermute_b32 v5, v41, v4
	s_waitcnt lgkmcnt(0)
	v_add_f32_e32 v4, v4, v5
	ds_bpermute_b32 v5, v42, v4
	s_waitcnt lgkmcnt(0)
	v_add_f32_e32 v4, v4, v5
	ds_bpermute_b32 v5, v43, v4
	s_waitcnt lgkmcnt(0)
	v_add_f32_e32 v4, v4, v5
	ds_bpermute_b32 v5, v44, v4
	s_waitcnt lgkmcnt(0)
	v_add_f32_e32 v4, v4, v5
	v_fmamk_f32 v4, v4, 0x3a000000, v212
	v_cmp_gt_f32_e32 vcc, s58, v4
	v_mul_f32_e32 v5, 0x4b800000, v4
	s_nop 0
	v_cndmask_b32_e32 v4, v4, v5, vcc
	v_rsq_f32_e32 v4, v4
	s_nop 0
	v_mul_f32_e32 v5, 0x45800000, v4
	v_cndmask_b32_e32 v26, v4, v5, vcc
	v_mov_b32_e32 v4, 0
	v_mov_b32_e32 v27, v26
	v_mov_b32_e32 v5, v4
	v_mov_b32_e32 v10, v4
	v_mov_b32_e32 v11, v4
	v_mov_b32_e32 v8, v4
	v_mov_b32_e32 v9, v4
	v_mov_b32_e32 v6, v4
	v_mov_b32_e32 v7, v4
.LBB6_1830:
	s_waitcnt vmcnt(0)
	v_lshl_add_u64 v[30:31], v[28:29], 0, v[16:17]
	v_add_co_u32_e32 v76, vcc, 0x200000, v30
	v_lshl_add_u64 v[34:35], s[6:7], 0, v[16:17]
	s_nop 0
	v_addc_co_u32_e32 v77, vcc, 0, v31, vcc
	v_add_co_u32_e32 v78, vcc, s79, v34
	v_mov_b64_e32 v[30:31], v[88:89]
	v_mov_b64_e32 v[32:33], v[90:91]
	s_nop 0
	v_addc_co_u32_e32 v79, vcc, 0, v35, vcc
	v_mov_b64_e32 v[34:35], v[120:121]
	v_mov_b64_e32 v[36:37], v[122:123]
	v_lshl_add_u64 v[38:39], v[14:15], 0, s[8:9]
	global_load_dwordx4 v[46:49], v[38:39], off offset:32
	global_load_dwordx4 v[50:53], v[38:39], off
	global_load_dwordx4 v[54:57], v[38:39], off offset:48
	global_load_dwordx4 v[58:61], v[38:39], off offset:16
	s_mov_b64 s[0:1], 0x2000
	s_add_u32 s8, s8, 0x4000
	s_addc_u32 s9, s9, 0
	s_add_u32 s6, s6, 0x800
	s_addc_u32 s7, s7, 0
	v_lshl_add_u64 v[28:29], v[28:29], 0, s[56:57]
	s_cmp_lg_u32 s8, 0x10000
	v_pk_mul_f32 v[30:31], v[26:27], v[30:31]
	v_pk_mul_f32 v[34:35], v[30:31], v[34:35]
	s_waitcnt vmcnt(1)
	v_mov_b32_e32 v31, v57
	s_waitcnt vmcnt(0)
	v_mul_f32_e32 v80, v34, v60
	v_mov_b32_e32 v30, v61
	global_load_dwordx4 v[60:63], v[38:39], off offset:112
	global_load_dwordx4 v[64:67], v[38:39], off offset:96
	global_load_dwordx4 v[68:71], v[38:39], off offset:64
	global_load_dwordx4 v[72:75], v[38:39], off offset:80
	v_pk_mul_f32 v[82:83], v[34:35], v[30:31]
	v_pk_fma_f32 v[10:11], v[34:35], v[50:51], v[10:11] op_sel_hi:[0,1,1]
	v_pk_mul_f32 v[30:31], v[26:27], v[32:33]
	v_pk_fma_f32 v[6:7], v[34:35], v[58:59], v[6:7] op_sel_hi:[0,1,1]
	v_pk_fma_f32 v[10:11], v[34:35], v[46:47], v[10:11] op_sel:[1,0,0]
	v_pk_mul_f32 v[46:47], v[30:31], v[36:37]
	v_pk_fma_f32 v[6:7], v[34:35], v[54:55], v[6:7] op_sel:[1,0,0]
	v_mov_b32_e32 v81, v82
	v_mul_f32_e32 v56, v35, v56
	v_pk_fma_f32 v[8:9], v[34:35], v[52:53], v[8:9] op_sel_hi:[0,1,1]
	v_pk_add_f32 v[4:5], v[4:5], v[80:81]
	v_mov_b32_e32 v57, v83
	v_pk_fma_f32 v[8:9], v[34:35], v[48:49], v[8:9] op_sel:[1,0,0]
	v_pk_add_f32 v[4:5], v[4:5], v[56:57]
	v_lshl_add_u64 v[58:59], v[38:39], 0, s[0:1]
	s_mov_b64 s[0:1], 0x2040
	s_waitcnt vmcnt(3)
	v_mov_b32_e32 v31, v63
	s_waitcnt vmcnt(1)
	v_pk_fma_f32 v[10:11], v[46:47], v[68:69], v[10:11] op_sel_hi:[0,1,1]
	s_waitcnt vmcnt(0)
	v_mov_b32_e32 v30, v75
	v_mul_f32_e32 v50, v46, v74
	v_pk_mul_f32 v[74:75], v[46:47], v[30:31]
	v_pk_fma_f32 v[6:7], v[46:47], v[72:73], v[6:7] op_sel_hi:[0,1,1]
	v_pk_fma_f32 v[32:33], v[46:47], v[60:61], v[6:7] op_sel:[1,0,0]
	v_mul_f32_e32 v6, v47, v62
	v_mov_b32_e32 v51, v74
	v_add_co_u32_e32 v62, vcc, s79, v38
	v_pk_fma_f32 v[8:9], v[46:47], v[70:71], v[8:9] op_sel_hi:[0,1,1]
	v_pk_add_f32 v[4:5], v[4:5], v[50:51]
	v_mov_b32_e32 v7, v75
	v_addc_co_u32_e32 v63, vcc, 0, v39, vcc
	v_pk_fma_f32 v[36:37], v[46:47], v[64:65], v[10:11] op_sel:[1,0,0]
	v_pk_fma_f32 v[30:31], v[46:47], v[66:67], v[8:9] op_sel:[1,0,0]
	v_pk_add_f32 v[34:35], v[4:5], v[6:7]
	v_mov_b64_e32 v[4:5], v[92:93]
	v_mov_b64_e32 v[6:7], v[94:95]
	v_mov_b64_e32 v[8:9], v[124:125]
	v_mov_b64_e32 v[10:11], v[126:127]
	global_load_dwordx4 v[46:49], v[62:63], off
	global_load_dwordx4 v[50:53], v[58:59], off offset:32
	global_load_dwordx4 v[54:57], v[58:59], off offset:48
	s_nop 0
	global_load_dwordx4 v[58:61], v[58:59], off offset:16
	v_pk_mul_f32 v[4:5], v[26:27], v[4:5]
	v_pk_mul_f32 v[4:5], v[4:5], v[8:9]
	s_waitcnt vmcnt(0)
	v_mov_b32_e32 v8, v61
	v_mov_b32_e32 v9, v57
	v_mul_f32_e32 v76, v4, v60
	v_pk_mul_f32 v[78:79], v[4:5], v[8:9]
	v_lshl_add_u64 v[8:9], v[38:39], 0, s[0:1]
	global_load_dwordx4 v[60:63], v[62:63], off offset:64
	s_nop 0
	global_load_dwordx4 v[64:67], v[8:9], off offset:48
	global_load_dwordx4 v[68:71], v[8:9], off offset:32
	global_load_dwordx4 v[72:75], v[8:9], off offset:16
	v_pk_fma_f32 v[8:9], v[4:5], v[46:47], v[36:37] op_sel_hi:[0,1,1]
	v_pk_mul_f32 v[6:7], v[26:27], v[6:7]
	v_pk_fma_f32 v[8:9], v[4:5], v[50:51], v[8:9] op_sel:[1,0,0]
	v_pk_mul_f32 v[36:37], v[6:7], v[10:11]
	v_mov_b32_e32 v77, v78
	v_mul_f32_e32 v56, v5, v56
	v_mov_b32_e32 v57, v79
	s_waitcnt vmcnt(2)
	v_mov_b32_e32 v7, v67
	s_waitcnt vmcnt(0)
	v_mov_b32_e32 v6, v75
	v_pk_mul_f32 v[46:47], v[36:37], v[6:7]
	v_pk_fma_f32 v[6:7], v[36:37], v[60:61], v[8:9] op_sel_hi:[0,1,1]
	v_pk_fma_f32 v[10:11], v[36:37], v[68:69], v[6:7] op_sel:[1,0,0]
	v_pk_fma_f32 v[6:7], v[4:5], v[48:49], v[30:31] op_sel_hi:[0,1,1]
	v_pk_fma_f32 v[6:7], v[4:5], v[52:53], v[6:7] op_sel:[1,0,0]
	v_pk_add_f32 v[30:31], v[34:35], v[76:77]
	v_pk_fma_f32 v[6:7], v[36:37], v[62:63], v[6:7] op_sel_hi:[0,1,1]
	v_pk_fma_f32 v[8:9], v[36:37], v[70:71], v[6:7] op_sel:[1,0,0]
	v_pk_fma_f32 v[6:7], v[4:5], v[58:59], v[32:33] op_sel_hi:[0,1,1]
	v_pk_fma_f32 v[4:5], v[4:5], v[54:55], v[6:7] op_sel:[1,0,0]
	v_mul_f32_e32 v38, v36, v74
	v_pk_fma_f32 v[4:5], v[36:37], v[72:73], v[4:5] op_sel_hi:[0,1,1]
	v_pk_add_f32 v[30:31], v[30:31], v[56:57]
	v_mov_b32_e32 v39, v46
	v_pk_fma_f32 v[6:7], v[36:37], v[64:65], v[4:5] op_sel:[1,0,0]
	v_mul_f32_e32 v4, v37, v66
	v_pk_add_f32 v[30:31], v[30:31], v[38:39]
	v_mov_b32_e32 v5, v47
	v_pk_add_f32 v[4:5], v[30:31], v[4:5]
	v_lshl_add_u64 v[30:31], v[28:29], 0, v[16:17]
	v_add_co_u32_e32 v76, vcc, 0x200000, v30
	v_lshl_add_u64 v[34:35], s[6:7], 0, v[16:17]
	s_nop 0
	v_addc_co_u32_e32 v77, vcc, 0, v31, vcc
	v_add_co_u32_e32 v78, vcc, s79, v34
	v_mov_b64_e32 v[30:31], v[96:97]
	v_mov_b64_e32 v[32:33], v[98:99]
	s_nop 0
	v_addc_co_u32_e32 v79, vcc, 0, v35, vcc
	v_mov_b64_e32 v[34:35], v[128:129]
	v_mov_b64_e32 v[36:37], v[130:131]
	v_lshl_add_u64 v[38:39], v[14:15], 0, s[8:9]
	global_load_dwordx4 v[46:49], v[38:39], off offset:32
	global_load_dwordx4 v[50:53], v[38:39], off
	global_load_dwordx4 v[54:57], v[38:39], off offset:48
	global_load_dwordx4 v[58:61], v[38:39], off offset:16
	s_mov_b64 s[0:1], 0x2000
	s_add_u32 s8, s8, 0x4000
	s_addc_u32 s9, s9, 0
	s_add_u32 s6, s6, 0x800
	s_addc_u32 s7, s7, 0
	v_lshl_add_u64 v[28:29], v[28:29], 0, s[56:57]
	s_cmp_lg_u32 s8, 0x10000
	v_pk_mul_f32 v[30:31], v[26:27], v[30:31]
	v_pk_mul_f32 v[34:35], v[30:31], v[34:35]
	s_waitcnt vmcnt(1)
	v_mov_b32_e32 v31, v57
	s_waitcnt vmcnt(0)
	v_mul_f32_e32 v80, v34, v60
	v_mov_b32_e32 v30, v61
	global_load_dwordx4 v[60:63], v[38:39], off offset:112
	global_load_dwordx4 v[64:67], v[38:39], off offset:96
	global_load_dwordx4 v[68:71], v[38:39], off offset:64
	global_load_dwordx4 v[72:75], v[38:39], off offset:80
	v_pk_mul_f32 v[82:83], v[34:35], v[30:31]
	v_pk_fma_f32 v[10:11], v[34:35], v[50:51], v[10:11] op_sel_hi:[0,1,1]
	v_pk_mul_f32 v[30:31], v[26:27], v[32:33]
	v_pk_fma_f32 v[6:7], v[34:35], v[58:59], v[6:7] op_sel_hi:[0,1,1]
	v_pk_fma_f32 v[10:11], v[34:35], v[46:47], v[10:11] op_sel:[1,0,0]
	v_pk_mul_f32 v[46:47], v[30:31], v[36:37]
	v_pk_fma_f32 v[6:7], v[34:35], v[54:55], v[6:7] op_sel:[1,0,0]
	v_mov_b32_e32 v81, v82
	v_mul_f32_e32 v56, v35, v56
	v_pk_fma_f32 v[8:9], v[34:35], v[52:53], v[8:9] op_sel_hi:[0,1,1]
	v_pk_add_f32 v[4:5], v[4:5], v[80:81]
	v_mov_b32_e32 v57, v83
	v_pk_fma_f32 v[8:9], v[34:35], v[48:49], v[8:9] op_sel:[1,0,0]
	v_pk_add_f32 v[4:5], v[4:5], v[56:57]
	v_lshl_add_u64 v[58:59], v[38:39], 0, s[0:1]
	s_mov_b64 s[0:1], 0x2040
	s_waitcnt vmcnt(3)
	v_mov_b32_e32 v31, v63
	s_waitcnt vmcnt(1)
	v_pk_fma_f32 v[10:11], v[46:47], v[68:69], v[10:11] op_sel_hi:[0,1,1]
	s_waitcnt vmcnt(0)
	v_mov_b32_e32 v30, v75
	v_mul_f32_e32 v50, v46, v74
	v_pk_mul_f32 v[74:75], v[46:47], v[30:31]
	v_pk_fma_f32 v[6:7], v[46:47], v[72:73], v[6:7] op_sel_hi:[0,1,1]
	v_pk_fma_f32 v[32:33], v[46:47], v[60:61], v[6:7] op_sel:[1,0,0]
	v_mul_f32_e32 v6, v47, v62
	v_mov_b32_e32 v51, v74
	v_add_co_u32_e32 v62, vcc, s79, v38
	v_pk_fma_f32 v[8:9], v[46:47], v[70:71], v[8:9] op_sel_hi:[0,1,1]
	v_pk_add_f32 v[4:5], v[4:5], v[50:51]
	v_mov_b32_e32 v7, v75
	v_addc_co_u32_e32 v63, vcc, 0, v39, vcc
	v_pk_fma_f32 v[36:37], v[46:47], v[64:65], v[10:11] op_sel:[1,0,0]
	v_pk_fma_f32 v[30:31], v[46:47], v[66:67], v[8:9] op_sel:[1,0,0]
	v_pk_add_f32 v[34:35], v[4:5], v[6:7]
	v_mov_b64_e32 v[4:5], v[100:101]
	v_mov_b64_e32 v[6:7], v[102:103]
	v_mov_b64_e32 v[8:9], v[132:133]
	v_mov_b64_e32 v[10:11], v[134:135]
	global_load_dwordx4 v[46:49], v[62:63], off
	global_load_dwordx4 v[50:53], v[58:59], off offset:32
	global_load_dwordx4 v[54:57], v[58:59], off offset:48
	s_nop 0
	global_load_dwordx4 v[58:61], v[58:59], off offset:16
	v_pk_mul_f32 v[4:5], v[26:27], v[4:5]
	v_pk_mul_f32 v[4:5], v[4:5], v[8:9]
	s_waitcnt vmcnt(0)
	v_mov_b32_e32 v8, v61
	v_mov_b32_e32 v9, v57
	v_mul_f32_e32 v76, v4, v60
	v_pk_mul_f32 v[78:79], v[4:5], v[8:9]
	v_lshl_add_u64 v[8:9], v[38:39], 0, s[0:1]
	global_load_dwordx4 v[60:63], v[62:63], off offset:64
	s_nop 0
	global_load_dwordx4 v[64:67], v[8:9], off offset:48
	global_load_dwordx4 v[68:71], v[8:9], off offset:32
	global_load_dwordx4 v[72:75], v[8:9], off offset:16
	v_pk_fma_f32 v[8:9], v[4:5], v[46:47], v[36:37] op_sel_hi:[0,1,1]
	v_pk_mul_f32 v[6:7], v[26:27], v[6:7]
	v_pk_fma_f32 v[8:9], v[4:5], v[50:51], v[8:9] op_sel:[1,0,0]
	v_pk_mul_f32 v[36:37], v[6:7], v[10:11]
	v_mov_b32_e32 v77, v78
	v_mul_f32_e32 v56, v5, v56
	v_mov_b32_e32 v57, v79
	s_waitcnt vmcnt(2)
	v_mov_b32_e32 v7, v67
	s_waitcnt vmcnt(0)
	v_mov_b32_e32 v6, v75
	v_pk_mul_f32 v[46:47], v[36:37], v[6:7]
	v_pk_fma_f32 v[6:7], v[36:37], v[60:61], v[8:9] op_sel_hi:[0,1,1]
	v_pk_fma_f32 v[10:11], v[36:37], v[68:69], v[6:7] op_sel:[1,0,0]
	v_pk_fma_f32 v[6:7], v[4:5], v[48:49], v[30:31] op_sel_hi:[0,1,1]
	v_pk_fma_f32 v[6:7], v[4:5], v[52:53], v[6:7] op_sel:[1,0,0]
	v_pk_add_f32 v[30:31], v[34:35], v[76:77]
	v_pk_fma_f32 v[6:7], v[36:37], v[62:63], v[6:7] op_sel_hi:[0,1,1]
	v_pk_fma_f32 v[8:9], v[36:37], v[70:71], v[6:7] op_sel:[1,0,0]
	v_pk_fma_f32 v[6:7], v[4:5], v[58:59], v[32:33] op_sel_hi:[0,1,1]
	v_pk_fma_f32 v[4:5], v[4:5], v[54:55], v[6:7] op_sel:[1,0,0]
	v_mul_f32_e32 v38, v36, v74
	v_pk_fma_f32 v[4:5], v[36:37], v[72:73], v[4:5] op_sel_hi:[0,1,1]
	v_pk_add_f32 v[30:31], v[30:31], v[56:57]
	v_mov_b32_e32 v39, v46
	v_pk_fma_f32 v[6:7], v[36:37], v[64:65], v[4:5] op_sel:[1,0,0]
	v_mul_f32_e32 v4, v37, v66
	v_pk_add_f32 v[30:31], v[30:31], v[38:39]
	v_mov_b32_e32 v5, v47
	v_pk_add_f32 v[4:5], v[30:31], v[4:5]
	v_lshl_add_u64 v[30:31], v[28:29], 0, v[16:17]
	v_add_co_u32_e32 v76, vcc, 0x200000, v30
	v_lshl_add_u64 v[34:35], s[6:7], 0, v[16:17]
	s_nop 0
	v_addc_co_u32_e32 v77, vcc, 0, v31, vcc
	v_add_co_u32_e32 v78, vcc, s79, v34
	v_mov_b64_e32 v[30:31], v[104:105]
	v_mov_b64_e32 v[32:33], v[106:107]
	s_nop 0
	v_addc_co_u32_e32 v79, vcc, 0, v35, vcc
	v_mov_b64_e32 v[34:35], v[136:137]
	v_mov_b64_e32 v[36:37], v[138:139]
	v_lshl_add_u64 v[38:39], v[14:15], 0, s[8:9]
	global_load_dwordx4 v[46:49], v[38:39], off offset:32
	global_load_dwordx4 v[50:53], v[38:39], off
	global_load_dwordx4 v[54:57], v[38:39], off offset:48
	global_load_dwordx4 v[58:61], v[38:39], off offset:16
	s_mov_b64 s[0:1], 0x2000
	s_add_u32 s8, s8, 0x4000
	s_addc_u32 s9, s9, 0
	s_add_u32 s6, s6, 0x800
	s_addc_u32 s7, s7, 0
	v_lshl_add_u64 v[28:29], v[28:29], 0, s[56:57]
	s_cmp_lg_u32 s8, 0x10000
	v_pk_mul_f32 v[30:31], v[26:27], v[30:31]
	v_pk_mul_f32 v[34:35], v[30:31], v[34:35]
	s_waitcnt vmcnt(1)
	v_mov_b32_e32 v31, v57
	s_waitcnt vmcnt(0)
	v_mul_f32_e32 v80, v34, v60
	v_mov_b32_e32 v30, v61
	global_load_dwordx4 v[60:63], v[38:39], off offset:112
	global_load_dwordx4 v[64:67], v[38:39], off offset:96
	global_load_dwordx4 v[68:71], v[38:39], off offset:64
	global_load_dwordx4 v[72:75], v[38:39], off offset:80
	v_pk_mul_f32 v[82:83], v[34:35], v[30:31]
	v_pk_fma_f32 v[10:11], v[34:35], v[50:51], v[10:11] op_sel_hi:[0,1,1]
	v_pk_mul_f32 v[30:31], v[26:27], v[32:33]
	v_pk_fma_f32 v[6:7], v[34:35], v[58:59], v[6:7] op_sel_hi:[0,1,1]
	v_pk_fma_f32 v[10:11], v[34:35], v[46:47], v[10:11] op_sel:[1,0,0]
	v_pk_mul_f32 v[46:47], v[30:31], v[36:37]
	v_pk_fma_f32 v[6:7], v[34:35], v[54:55], v[6:7] op_sel:[1,0,0]
	v_mov_b32_e32 v81, v82
	v_mul_f32_e32 v56, v35, v56
	v_pk_fma_f32 v[8:9], v[34:35], v[52:53], v[8:9] op_sel_hi:[0,1,1]
	v_pk_add_f32 v[4:5], v[4:5], v[80:81]
	v_mov_b32_e32 v57, v83
	v_pk_fma_f32 v[8:9], v[34:35], v[48:49], v[8:9] op_sel:[1,0,0]
	v_pk_add_f32 v[4:5], v[4:5], v[56:57]
	v_lshl_add_u64 v[58:59], v[38:39], 0, s[0:1]
	s_mov_b64 s[0:1], 0x2040
	s_waitcnt vmcnt(3)
	v_mov_b32_e32 v31, v63
	s_waitcnt vmcnt(1)
	v_pk_fma_f32 v[10:11], v[46:47], v[68:69], v[10:11] op_sel_hi:[0,1,1]
	s_waitcnt vmcnt(0)
	v_mov_b32_e32 v30, v75
	v_mul_f32_e32 v50, v46, v74
	v_pk_mul_f32 v[74:75], v[46:47], v[30:31]
	v_pk_fma_f32 v[6:7], v[46:47], v[72:73], v[6:7] op_sel_hi:[0,1,1]
	v_pk_fma_f32 v[32:33], v[46:47], v[60:61], v[6:7] op_sel:[1,0,0]
	v_mul_f32_e32 v6, v47, v62
	v_mov_b32_e32 v51, v74
	v_add_co_u32_e32 v62, vcc, s79, v38
	v_pk_fma_f32 v[8:9], v[46:47], v[70:71], v[8:9] op_sel_hi:[0,1,1]
	v_pk_add_f32 v[4:5], v[4:5], v[50:51]
	v_mov_b32_e32 v7, v75
	v_addc_co_u32_e32 v63, vcc, 0, v39, vcc
	v_pk_fma_f32 v[36:37], v[46:47], v[64:65], v[10:11] op_sel:[1,0,0]
	v_pk_fma_f32 v[30:31], v[46:47], v[66:67], v[8:9] op_sel:[1,0,0]
	v_pk_add_f32 v[34:35], v[4:5], v[6:7]
	v_mov_b64_e32 v[4:5], v[108:109]
	v_mov_b64_e32 v[6:7], v[110:111]
	v_mov_b64_e32 v[8:9], v[140:141]
	v_mov_b64_e32 v[10:11], v[142:143]
	global_load_dwordx4 v[46:49], v[62:63], off
	global_load_dwordx4 v[50:53], v[58:59], off offset:32
	global_load_dwordx4 v[54:57], v[58:59], off offset:48
	s_nop 0
	global_load_dwordx4 v[58:61], v[58:59], off offset:16
	v_pk_mul_f32 v[4:5], v[26:27], v[4:5]
	v_pk_mul_f32 v[4:5], v[4:5], v[8:9]
	s_waitcnt vmcnt(0)
	v_mov_b32_e32 v8, v61
	v_mov_b32_e32 v9, v57
	v_mul_f32_e32 v76, v4, v60
	v_pk_mul_f32 v[78:79], v[4:5], v[8:9]
	v_lshl_add_u64 v[8:9], v[38:39], 0, s[0:1]
	global_load_dwordx4 v[60:63], v[62:63], off offset:64
	s_nop 0
	global_load_dwordx4 v[64:67], v[8:9], off offset:48
	global_load_dwordx4 v[68:71], v[8:9], off offset:32
	global_load_dwordx4 v[72:75], v[8:9], off offset:16
	v_pk_fma_f32 v[8:9], v[4:5], v[46:47], v[36:37] op_sel_hi:[0,1,1]
	v_pk_mul_f32 v[6:7], v[26:27], v[6:7]
	v_pk_fma_f32 v[8:9], v[4:5], v[50:51], v[8:9] op_sel:[1,0,0]
	v_pk_mul_f32 v[36:37], v[6:7], v[10:11]
	v_mov_b32_e32 v77, v78
	v_mul_f32_e32 v56, v5, v56
	v_mov_b32_e32 v57, v79
	s_waitcnt vmcnt(2)
	v_mov_b32_e32 v7, v67
	s_waitcnt vmcnt(0)
	v_mov_b32_e32 v6, v75
	v_pk_mul_f32 v[46:47], v[36:37], v[6:7]
	v_pk_fma_f32 v[6:7], v[36:37], v[60:61], v[8:9] op_sel_hi:[0,1,1]
	v_pk_fma_f32 v[10:11], v[36:37], v[68:69], v[6:7] op_sel:[1,0,0]
	v_pk_fma_f32 v[6:7], v[4:5], v[48:49], v[30:31] op_sel_hi:[0,1,1]
	v_pk_fma_f32 v[6:7], v[4:5], v[52:53], v[6:7] op_sel:[1,0,0]
	v_pk_add_f32 v[30:31], v[34:35], v[76:77]
	v_pk_fma_f32 v[6:7], v[36:37], v[62:63], v[6:7] op_sel_hi:[0,1,1]
	v_pk_fma_f32 v[8:9], v[36:37], v[70:71], v[6:7] op_sel:[1,0,0]
	v_pk_fma_f32 v[6:7], v[4:5], v[58:59], v[32:33] op_sel_hi:[0,1,1]
	v_pk_fma_f32 v[4:5], v[4:5], v[54:55], v[6:7] op_sel:[1,0,0]
	v_mul_f32_e32 v38, v36, v74
	v_pk_fma_f32 v[4:5], v[36:37], v[72:73], v[4:5] op_sel_hi:[0,1,1]
	v_pk_add_f32 v[30:31], v[30:31], v[56:57]
	v_mov_b32_e32 v39, v46
	v_pk_fma_f32 v[6:7], v[36:37], v[64:65], v[4:5] op_sel:[1,0,0]
	v_mul_f32_e32 v4, v37, v66
	v_pk_add_f32 v[30:31], v[30:31], v[38:39]
	v_mov_b32_e32 v5, v47
	v_pk_add_f32 v[4:5], v[30:31], v[4:5]
	v_lshl_add_u64 v[30:31], v[28:29], 0, v[16:17]
	v_add_co_u32_e32 v76, vcc, 0x200000, v30
	v_lshl_add_u64 v[34:35], s[6:7], 0, v[16:17]
	s_nop 0
	v_addc_co_u32_e32 v77, vcc, 0, v31, vcc
	v_add_co_u32_e32 v78, vcc, s79, v34
	v_mov_b64_e32 v[30:31], v[112:113]
	v_mov_b64_e32 v[32:33], v[114:115]
	s_nop 0
	v_addc_co_u32_e32 v79, vcc, 0, v35, vcc
	v_mov_b64_e32 v[34:35], v[144:145]
	v_mov_b64_e32 v[36:37], v[146:147]
	v_lshl_add_u64 v[38:39], v[14:15], 0, s[8:9]
	global_load_dwordx4 v[46:49], v[38:39], off offset:32
	global_load_dwordx4 v[50:53], v[38:39], off
	global_load_dwordx4 v[54:57], v[38:39], off offset:48
	global_load_dwordx4 v[58:61], v[38:39], off offset:16
	s_mov_b64 s[0:1], 0x2000
	s_add_u32 s8, s8, 0x4000
	s_addc_u32 s9, s9, 0
	s_add_u32 s6, s6, 0x800
	s_addc_u32 s7, s7, 0
	v_lshl_add_u64 v[28:29], v[28:29], 0, s[56:57]
	s_cmp_lg_u32 s8, 0x10000
	v_pk_mul_f32 v[30:31], v[26:27], v[30:31]
	v_pk_mul_f32 v[34:35], v[30:31], v[34:35]
	s_waitcnt vmcnt(1)
	v_mov_b32_e32 v31, v57
	s_waitcnt vmcnt(0)
	v_mul_f32_e32 v80, v34, v60
	v_mov_b32_e32 v30, v61
	global_load_dwordx4 v[60:63], v[38:39], off offset:112
	global_load_dwordx4 v[64:67], v[38:39], off offset:96
	global_load_dwordx4 v[68:71], v[38:39], off offset:64
	global_load_dwordx4 v[72:75], v[38:39], off offset:80
	v_pk_mul_f32 v[82:83], v[34:35], v[30:31]
	v_pk_fma_f32 v[10:11], v[34:35], v[50:51], v[10:11] op_sel_hi:[0,1,1]
	v_pk_mul_f32 v[30:31], v[26:27], v[32:33]
	v_pk_fma_f32 v[6:7], v[34:35], v[58:59], v[6:7] op_sel_hi:[0,1,1]
	v_pk_fma_f32 v[10:11], v[34:35], v[46:47], v[10:11] op_sel:[1,0,0]
	v_pk_mul_f32 v[46:47], v[30:31], v[36:37]
	v_pk_fma_f32 v[6:7], v[34:35], v[54:55], v[6:7] op_sel:[1,0,0]
	v_mov_b32_e32 v81, v82
	v_mul_f32_e32 v56, v35, v56
	v_pk_fma_f32 v[8:9], v[34:35], v[52:53], v[8:9] op_sel_hi:[0,1,1]
	v_pk_add_f32 v[4:5], v[4:5], v[80:81]
	v_mov_b32_e32 v57, v83
	v_pk_fma_f32 v[8:9], v[34:35], v[48:49], v[8:9] op_sel:[1,0,0]
	v_pk_add_f32 v[4:5], v[4:5], v[56:57]
	v_lshl_add_u64 v[58:59], v[38:39], 0, s[0:1]
	s_mov_b64 s[0:1], 0x2040
	s_waitcnt vmcnt(3)
	v_mov_b32_e32 v31, v63
	s_waitcnt vmcnt(1)
	v_pk_fma_f32 v[10:11], v[46:47], v[68:69], v[10:11] op_sel_hi:[0,1,1]
	s_waitcnt vmcnt(0)
	v_mov_b32_e32 v30, v75
	v_mul_f32_e32 v50, v46, v74
	v_pk_mul_f32 v[74:75], v[46:47], v[30:31]
	v_pk_fma_f32 v[6:7], v[46:47], v[72:73], v[6:7] op_sel_hi:[0,1,1]
	v_pk_fma_f32 v[32:33], v[46:47], v[60:61], v[6:7] op_sel:[1,0,0]
	v_mul_f32_e32 v6, v47, v62
	v_mov_b32_e32 v51, v74
	v_add_co_u32_e32 v62, vcc, s79, v38
	v_pk_fma_f32 v[8:9], v[46:47], v[70:71], v[8:9] op_sel_hi:[0,1,1]
	v_pk_add_f32 v[4:5], v[4:5], v[50:51]
	v_mov_b32_e32 v7, v75
	v_addc_co_u32_e32 v63, vcc, 0, v39, vcc
	v_pk_fma_f32 v[36:37], v[46:47], v[64:65], v[10:11] op_sel:[1,0,0]
	v_pk_fma_f32 v[30:31], v[46:47], v[66:67], v[8:9] op_sel:[1,0,0]
	v_pk_add_f32 v[34:35], v[4:5], v[6:7]
	v_mov_b64_e32 v[4:5], v[116:117]
	v_mov_b64_e32 v[6:7], v[118:119]
	v_mov_b64_e32 v[8:9], v[148:149]
	v_mov_b64_e32 v[10:11], v[150:151]
	global_load_dwordx4 v[46:49], v[62:63], off
	global_load_dwordx4 v[50:53], v[58:59], off offset:32
	global_load_dwordx4 v[54:57], v[58:59], off offset:48
	s_nop 0
	global_load_dwordx4 v[58:61], v[58:59], off offset:16
	v_pk_mul_f32 v[4:5], v[26:27], v[4:5]
	v_pk_mul_f32 v[4:5], v[4:5], v[8:9]
	s_waitcnt vmcnt(0)
	v_mov_b32_e32 v8, v61
	v_mov_b32_e32 v9, v57
	v_mul_f32_e32 v76, v4, v60
	v_pk_mul_f32 v[78:79], v[4:5], v[8:9]
	v_lshl_add_u64 v[8:9], v[38:39], 0, s[0:1]
	global_load_dwordx4 v[60:63], v[62:63], off offset:64
	s_nop 0
	global_load_dwordx4 v[64:67], v[8:9], off offset:48
	global_load_dwordx4 v[68:71], v[8:9], off offset:32
	global_load_dwordx4 v[72:75], v[8:9], off offset:16
	v_pk_fma_f32 v[8:9], v[4:5], v[46:47], v[36:37] op_sel_hi:[0,1,1]
	v_pk_mul_f32 v[6:7], v[26:27], v[6:7]
	v_pk_fma_f32 v[8:9], v[4:5], v[50:51], v[8:9] op_sel:[1,0,0]
	v_pk_mul_f32 v[36:37], v[6:7], v[10:11]
	v_mov_b32_e32 v77, v78
	v_mul_f32_e32 v56, v5, v56
	v_mov_b32_e32 v57, v79
	s_waitcnt vmcnt(2)
	v_mov_b32_e32 v7, v67
	s_waitcnt vmcnt(0)
	v_mov_b32_e32 v6, v75
	v_pk_mul_f32 v[46:47], v[36:37], v[6:7]
	v_pk_fma_f32 v[6:7], v[36:37], v[60:61], v[8:9] op_sel_hi:[0,1,1]
	v_pk_fma_f32 v[10:11], v[36:37], v[68:69], v[6:7] op_sel:[1,0,0]
	v_pk_fma_f32 v[6:7], v[4:5], v[48:49], v[30:31] op_sel_hi:[0,1,1]
	v_pk_fma_f32 v[6:7], v[4:5], v[52:53], v[6:7] op_sel:[1,0,0]
	v_pk_add_f32 v[30:31], v[34:35], v[76:77]
	v_pk_fma_f32 v[6:7], v[36:37], v[62:63], v[6:7] op_sel_hi:[0,1,1]
	v_pk_fma_f32 v[8:9], v[36:37], v[70:71], v[6:7] op_sel:[1,0,0]
	v_pk_fma_f32 v[6:7], v[4:5], v[58:59], v[32:33] op_sel_hi:[0,1,1]
	v_pk_fma_f32 v[4:5], v[4:5], v[54:55], v[6:7] op_sel:[1,0,0]
	v_mul_f32_e32 v38, v36, v74
	v_pk_fma_f32 v[4:5], v[36:37], v[72:73], v[4:5] op_sel_hi:[0,1,1]
	v_pk_add_f32 v[30:31], v[30:31], v[56:57]
	v_mov_b32_e32 v39, v46
	v_pk_fma_f32 v[6:7], v[36:37], v[64:65], v[4:5] op_sel:[1,0,0]
	v_mul_f32_e32 v4, v37, v66
	v_pk_add_f32 v[30:31], v[30:31], v[38:39]
	v_mov_b32_e32 v5, v47
	v_pk_add_f32 v[4:5], v[30:31], v[4:5]
	ds_bpermute_b32 v27, v25, v8
	ds_bpermute_b32 v28, v25, v10
	ds_bpermute_b32 v29, v25, v11
	s_mov_b32 s0, 0xff800000
	s_waitcnt lgkmcnt(2)
	v_add_f32_e32 v8, v8, v27
	ds_bpermute_b32 v27, v40, v8
	s_waitcnt lgkmcnt(1)
	v_pk_add_f32 v[10:11], v[10:11], v[28:29]
	ds_bpermute_b32 v28, v40, v10
	ds_bpermute_b32 v29, v40, v11
	s_waitcnt lgkmcnt(2)
	v_add_f32_e32 v8, v8, v27
	ds_bpermute_b32 v27, v41, v8
	s_waitcnt lgkmcnt(1)
	v_pk_add_f32 v[10:11], v[10:11], v[28:29]
	ds_bpermute_b32 v28, v41, v10
	ds_bpermute_b32 v29, v41, v11
	s_waitcnt lgkmcnt(2)
	v_add_f32_e32 v8, v8, v27
	ds_bpermute_b32 v27, v42, v8
	s_waitcnt lgkmcnt(1)
	v_pk_add_f32 v[10:11], v[10:11], v[28:29]
	ds_bpermute_b32 v28, v42, v10
	s_waitcnt lgkmcnt(1)
	v_add_f32_e32 v8, v8, v27
	ds_bpermute_b32 v27, v43, v8
	ds_bpermute_b32 v29, v42, v11
	s_waitcnt lgkmcnt(1)
	v_add_f32_e32 v8, v8, v27
	ds_bpermute_b32 v27, v44, v8
	s_waitcnt lgkmcnt(1)
	v_pk_add_f32 v[10:11], v[10:11], v[28:29]
	ds_bpermute_b32 v28, v43, v10
	ds_bpermute_b32 v29, v43, v11
	s_waitcnt lgkmcnt(2)
	v_add_f32_e32 v8, v8, v27
	ds_bpermute_b32 v27, v25, v9
	s_waitcnt lgkmcnt(1)
	v_pk_add_f32 v[10:11], v[10:11], v[28:29]
	ds_bpermute_b32 v28, v44, v10
	ds_bpermute_b32 v29, v44, v11
	s_waitcnt lgkmcnt(2)
	v_add_f32_e32 v9, v9, v27
	ds_bpermute_b32 v27, v40, v9
	s_waitcnt lgkmcnt(1)
	v_pk_add_f32 v[10:11], v[10:11], v[28:29]
	s_nop 0
	v_cmp_gt_f32_e32 vcc, v11, v10
	s_waitcnt lgkmcnt(0)
	v_add_f32_e32 v9, v9, v27
	ds_bpermute_b32 v27, v41, v9
	v_cmp_nlg_f32_e64 s[10:11], s0, v10
	s_waitcnt lgkmcnt(0)
	v_add_f32_e32 v9, v9, v27
	ds_bpermute_b32 v27, v42, v9
	s_waitcnt lgkmcnt(0)
	v_add_f32_e32 v9, v9, v27
	ds_bpermute_b32 v27, v43, v9
	s_waitcnt lgkmcnt(0)
	v_add_f32_e32 v9, v9, v27
	ds_bpermute_b32 v27, v44, v9
	s_waitcnt lgkmcnt(0)
	v_add_f32_e32 v9, v9, v27
	ds_bpermute_b32 v27, v25, v6
	s_waitcnt lgkmcnt(0)
	v_add_f32_e32 v6, v6, v27
	ds_bpermute_b32 v27, v40, v6
	s_waitcnt lgkmcnt(0)
	v_add_f32_e32 v6, v6, v27
	ds_bpermute_b32 v27, v41, v6
	s_waitcnt lgkmcnt(0)
	v_add_f32_e32 v6, v6, v27
	ds_bpermute_b32 v27, v42, v6
	s_waitcnt lgkmcnt(0)
	v_add_f32_e32 v6, v6, v27
	ds_bpermute_b32 v27, v43, v6
	s_waitcnt lgkmcnt(0)
	v_add_f32_e32 v6, v6, v27
	ds_bpermute_b32 v27, v44, v6
	s_waitcnt lgkmcnt(0)
	v_add_f32_e32 v27, v6, v27
	ds_bpermute_b32 v6, v25, v7
	s_waitcnt lgkmcnt(0)
	v_add_f32_e32 v6, v7, v6
	ds_bpermute_b32 v7, v40, v6
	s_waitcnt lgkmcnt(0)
	v_add_f32_e32 v6, v6, v7
	ds_bpermute_b32 v7, v41, v6
	s_waitcnt lgkmcnt(0)
	v_add_f32_e32 v6, v6, v7
	ds_bpermute_b32 v7, v42, v6
	s_waitcnt lgkmcnt(0)
	v_add_f32_e32 v6, v6, v7
	ds_bpermute_b32 v7, v43, v6
	s_waitcnt lgkmcnt(0)
	v_add_f32_e32 v6, v6, v7
	ds_bpermute_b32 v7, v44, v6
	s_waitcnt lgkmcnt(0)
	v_add_f32_e32 v28, v6, v7
	ds_bpermute_b32 v6, v25, v4
	s_waitcnt lgkmcnt(0)
	v_add_f32_e32 v4, v4, v6
	ds_bpermute_b32 v6, v40, v4
	s_waitcnt lgkmcnt(0)
	v_add_f32_e32 v4, v4, v6
	ds_bpermute_b32 v6, v41, v4
	s_waitcnt lgkmcnt(0)
	v_add_f32_e32 v4, v4, v6
	ds_bpermute_b32 v6, v42, v4
	s_waitcnt lgkmcnt(0)
	v_add_f32_e32 v4, v4, v6
	ds_bpermute_b32 v6, v43, v4
	s_waitcnt lgkmcnt(0)
	v_add_f32_e32 v4, v4, v6
	ds_bpermute_b32 v6, v44, v4
	s_waitcnt lgkmcnt(0)
	v_add_f32_e32 v29, v4, v6
	ds_bpermute_b32 v4, v25, v5
	s_waitcnt lgkmcnt(0)
	v_add_f32_e32 v4, v5, v4
	ds_bpermute_b32 v5, v40, v4
	s_waitcnt lgkmcnt(0)
	v_add_f32_e32 v4, v4, v5
	ds_bpermute_b32 v5, v41, v4
	s_waitcnt lgkmcnt(0)
	v_add_f32_e32 v4, v4, v5
	ds_bpermute_b32 v5, v42, v4
	s_waitcnt lgkmcnt(0)
	v_add_f32_e32 v4, v4, v5
	ds_bpermute_b32 v5, v43, v4
	s_waitcnt lgkmcnt(0)
	v_add_f32_e32 v4, v4, v5
	ds_bpermute_b32 v5, v44, v4
	s_waitcnt lgkmcnt(0)
	v_add_f32_e32 v6, v4, v5
	v_cndmask_b32_e32 v5, v10, v11, vcc
	v_cndmask_b32_e64 v4, 0, 1, vcc
	v_cmp_gt_f32_e32 vcc, v8, v5
	s_nop 1
	v_cndmask_b32_e32 v5, v5, v8, vcc
	v_cndmask_b32_e64 v4, v4, 2, vcc
	v_cmp_gt_f32_e32 vcc, v9, v5
	s_nop 1
	v_cndmask_b32_e32 v5, v5, v9, vcc
	v_cndmask_b32_e64 v4, v4, 3, vcc
	v_cmp_gt_f32_e32 vcc, v27, v5
	s_nop 1
	v_cndmask_b32_e32 v5, v5, v27, vcc
	v_cndmask_b32_e64 v4, v4, 4, vcc
	v_cmp_gt_f32_e32 vcc, v28, v5
	s_nop 1
	v_cndmask_b32_e32 v5, v5, v28, vcc
	v_cmp_gt_f32_e64 s[6:7], v29, v5
	v_cndmask_b32_e64 v4, v4, 5, vcc
	s_nop 0
	v_cndmask_b32_e64 v7, v5, v29, s[6:7]
	v_cndmask_b32_e64 v4, v4, 6, s[6:7]
	v_cmp_ngt_f32_e32 vcc, v6, v7
	s_and_b64 s[0:1], s[6:7], vcc
	s_nop 0
	v_cndmask_b32_e32 v4, 7, v4, vcc
	v_cmp_eq_u32_e64 s[8:9], 0, v4
	s_or_b64 s[8:9], s[8:9], s[10:11]
	s_nop 0
	v_cndmask_b32_e64 v10, v10, v226, s[8:9]
	v_cndmask_b32_e64 v5, 0, -1, s[8:9]
	v_cmp_ne_u32_e64 s[8:9], 1, v4
	v_cmp_gt_f32_e64 s[10:11], v11, v10
	s_and_b64 s[8:9], s[8:9], s[10:11]
	v_cndmask_b32_e64 v10, v10, v11, s[8:9]
	v_cndmask_b32_e64 v5, v5, 1, s[8:9]
	v_cmp_ne_u32_e64 s[8:9], 2, v4
	v_cmp_gt_f32_e64 s[10:11], v8, v10
	s_and_b64 s[8:9], s[8:9], s[10:11]
	v_cndmask_b32_e64 v8, v10, v8, s[8:9]
	v_cndmask_b32_e64 v5, v5, 2, s[8:9]
	v_cmp_ne_u32_e64 s[8:9], 3, v4
	v_cmp_gt_f32_e64 s[10:11], v9, v8
	s_and_b64 s[8:9], s[8:9], s[10:11]
	v_cndmask_b32_e64 v8, v8, v9, s[8:9]
	v_cndmask_b32_e64 v5, v5, 3, s[8:9]
	v_cmp_ne_u32_e64 s[8:9], 4, v4
	v_cmp_gt_f32_e64 s[10:11], v27, v8
	s_and_b64 s[8:9], s[8:9], s[10:11]
	v_cndmask_b32_e64 v8, v8, v27, s[8:9]
	v_cndmask_b32_e64 v5, v5, 4, s[8:9]
	v_cmp_ne_u32_e64 s[8:9], 5, v4
	v_cmp_gt_f32_e64 s[10:11], v28, v8
	s_and_b64 s[8:9], s[8:9], s[10:11]
	v_cndmask_b32_e64 v8, v8, v28, s[8:9]
	v_cmp_ngt_f32_e64 s[6:7], v29, v8
	s_or_b64 s[6:7], s[0:1], s[6:7]
	v_cndmask_b32_e64 v5, v5, 5, s[8:9]
	v_cndmask_b32_e64 v11, v29, v8, s[6:7]
	v_cndmask_b32_e64 v5, 6, v5, s[6:7]
	v_cmp_gt_f32_e64 s[6:7], v6, v11
	s_and_b64 s[6:7], vcc, s[6:7]
	s_nop 0
	v_cndmask_b32_e64 v8, v5, 7, s[6:7]
	v_ashrrev_i32_e32 v9, 31, v8
	s_and_saveexec_b64 s[0:1], s[4:5]
	s_xor_b64 s[8:9], exec, s[0:1]
	s_or_saveexec_b64 s[8:9], s[8:9]
	v_mov_b32_e32 v5, 0
	v_mov_b32_e32 v10, 0
	s_xor_b64 exec, exec, s[8:9]
	s_cbranch_execz .LBB6_1835
	v_cndmask_b32_e64 v5, v11, v6, s[6:7]
	v_cndmask_b32_e32 v6, v6, v7, vcc
	v_sub_f32_e32 v5, v5, v6
	v_mul_f32_e32 v5, 0x3fb8aa3b, v5
	v_exp_f32_e32 v5, v5
	v_mov_b32_e32 v215, 1
	v_add_f32_e32 v6, 1.0, v5
	v_div_scale_f32 v7, s[0:1], v6, v6, 1.0
	v_rcp_f32_e32 v10, v7
	v_readlane_b32 s0, v254, 16
	v_readlane_b32 s1, v254, 17
	v_fma_f32 v11, -v7, v10, 1.0
	v_fmac_f32_e32 v10, v11, v10
	v_div_scale_f32 v11, vcc, 1.0, v6, 1.0
	v_mul_f32_e32 v27, v11, v10
	v_fma_f32 v28, -v7, v27, v11
	v_fmac_f32_e32 v27, v28, v10
	v_fma_f32 v7, -v7, v27, v11
	v_div_fmas_f32 v7, v7, v10, v27
	v_div_fixup_f32 v6, v7, v6, 1.0
	v_mul_f32_e32 v11, v5, v6
	v_mov_b32_e32 v5, v3
	v_lshl_add_u64 v[28:29], v[4:5], 2, s[0:1]
	v_mov_b32_e32 v7, 1
	global_atomic_add v5, v[28:29], v7, off sc0
	v_lshl_add_u64 v[28:29], v[8:9], 2, s[0:1]
	global_atomic_add v10, v[28:29], v7, off sc0
	v_readlane_b32 s0, v254, 18
	v_lshlrev_b64 v[28:29], 5, v[12:13]
	v_readlane_b32 s1, v254, 19
	v_mov_b32_e32 v7, v8
	s_nop 0
	v_lshl_add_u64 v[28:29], s[0:1], 0, v[28:29]
	s_waitcnt vmcnt(1)
	global_store_dwordx4 v[28:29], v[4:7], off
	s_waitcnt vmcnt(1)
	global_store_dwordx2 v[28:29], v[10:11], off offset:16

.LBB6_1836:
	v_lshl_add_u64 v[26:27], s[38:39], 0, v[8:9]
	v_add_co_u32_e32 v34, vcc, 0x200000, v26
	v_lshl_add_u64 v[30:31], v[22:23], 0, s[6:7]
	s_nop 0
	v_addc_co_u32_e32 v35, vcc, 0, v27, vcc
	v_add_co_u32_e32 v36, vcc, 0x2000, v30
	v_mov_b64_e32 v[26:27], v[88:89]
	v_mov_b64_e32 v[28:29], v[90:91]
	s_nop 0
	v_addc_co_u32_e32 v37, vcc, 0, v31, vcc
	v_mov_b64_e32 v[30:31], v[120:121]
	v_mov_b64_e32 v[32:33], v[122:123]
	s_add_u32 s6, s6, 0x800
	s_addc_u32 s7, s7, 0
	v_lshl_add_u64 v[8:9], v[8:9], 0, s[56:57]
	s_cmpk_eq_i32 s6, 0x2000
	v_mul_f32_e32 v11, v10, v26
	v_mul_f32_e32 v13, v10, v27
	v_mul_f32_e32 v26, v10, v28
	v_mul_f32_e32 v11, v11, v30
	v_mul_f32_e32 v13, v13, v31
	v_mov_b32_e32 v28, v3
	v_cvt_pk_fp8_f32 v28, v11, v13
	v_mul_f32_e32 v27, v10, v29
	v_mul_f32_e32 v26, v26, v32
	v_mul_f32_e32 v27, v27, v33
	v_cvt_pk_fp8_f32 v28, v26, v27 op_sel:[0,0,1]
	v_lshl_add_u64 v[26:27], s[38:39], 0, v[4:5]
	v_add_co_u32_e32 v38, vcc, s72, v26
	v_lshl_add_u64 v[4:5], v[4:5], 0, s[88:89]
	s_nop 0
	v_addc_co_u32_e32 v39, vcc, 0, v27, vcc
	v_lshl_add_u64 v[26:27], s[38:39], 0, v[6:7]
	v_add_co_u32_e32 v46, vcc, s72, v26
	global_store_dword v[38:39], v28, off
	s_nop 0
	v_addc_co_u32_e32 v47, vcc, 0, v27, vcc
	global_store_dword v[46:47], v28, off
	v_mov_b64_e32 v[26:27], v[92:93]
	v_mov_b64_e32 v[28:29], v[94:95]
	s_nop 0
	v_mov_b64_e32 v[30:31], v[124:125]
	v_mov_b64_e32 v[32:33], v[126:127]
	v_lshl_add_u64 v[6:7], v[6:7], 0, s[88:89]
	v_mul_f32_e32 v11, v10, v26
	v_mul_f32_e32 v13, v10, v27
	v_mul_f32_e32 v11, v11, v30
	v_mul_f32_e32 v13, v13, v31
	v_mul_f32_e32 v26, v10, v28
	v_mov_b32_e32 v28, v3
	v_cvt_pk_fp8_f32 v28, v11, v13
	v_mul_f32_e32 v27, v10, v29
	v_mul_f32_e32 v26, v26, v32
	v_mul_f32_e32 v27, v27, v33
	v_cvt_pk_fp8_f32 v28, v26, v27 op_sel:[0,0,1]
	global_store_dword v[38:39], v28, off offset:256
	global_store_dword v[46:47], v28, off offset:256
	v_lshl_add_u64 v[26:27], s[38:39], 0, v[8:9]
	v_add_co_u32_e32 v34, vcc, 0x200000, v26
	v_lshl_add_u64 v[30:31], v[22:23], 0, s[6:7]
	s_nop 0
	v_addc_co_u32_e32 v35, vcc, 0, v27, vcc
	v_add_co_u32_e32 v36, vcc, 0x2000, v30
	v_mov_b64_e32 v[26:27], v[96:97]
	v_mov_b64_e32 v[28:29], v[98:99]
	s_nop 0
	v_addc_co_u32_e32 v37, vcc, 0, v31, vcc
	v_mov_b64_e32 v[30:31], v[128:129]
	v_mov_b64_e32 v[32:33], v[130:131]
	s_add_u32 s6, s6, 0x800
	s_addc_u32 s7, s7, 0
	v_lshl_add_u64 v[8:9], v[8:9], 0, s[56:57]
	s_cmpk_eq_i32 s6, 0x2000
	v_mul_f32_e32 v11, v10, v26
	v_mul_f32_e32 v13, v10, v27
	v_mul_f32_e32 v26, v10, v28
	v_mul_f32_e32 v11, v11, v30
	v_mul_f32_e32 v13, v13, v31
	v_mov_b32_e32 v28, v3
	v_cvt_pk_fp8_f32 v28, v11, v13
	v_mul_f32_e32 v27, v10, v29
	v_mul_f32_e32 v26, v26, v32
	v_mul_f32_e32 v27, v27, v33
	v_cvt_pk_fp8_f32 v28, v26, v27 op_sel:[0,0,1]
	v_lshl_add_u64 v[26:27], s[38:39], 0, v[4:5]
	v_add_co_u32_e32 v38, vcc, s72, v26
	v_lshl_add_u64 v[4:5], v[4:5], 0, s[88:89]
	s_nop 0
	v_addc_co_u32_e32 v39, vcc, 0, v27, vcc
	v_lshl_add_u64 v[26:27], s[38:39], 0, v[6:7]
	v_add_co_u32_e32 v46, vcc, s72, v26
	global_store_dword v[38:39], v28, off
	s_nop 0
	v_addc_co_u32_e32 v47, vcc, 0, v27, vcc
	global_store_dword v[46:47], v28, off
	v_mov_b64_e32 v[26:27], v[100:101]
	v_mov_b64_e32 v[28:29], v[102:103]
	s_nop 0
	v_mov_b64_e32 v[30:31], v[132:133]
	v_mov_b64_e32 v[32:33], v[134:135]
	v_lshl_add_u64 v[6:7], v[6:7], 0, s[88:89]
	v_mul_f32_e32 v11, v10, v26
	v_mul_f32_e32 v13, v10, v27
	v_mul_f32_e32 v11, v11, v30
	v_mul_f32_e32 v13, v13, v31
	v_mul_f32_e32 v26, v10, v28
	v_mov_b32_e32 v28, v3
	v_cvt_pk_fp8_f32 v28, v11, v13
	v_mul_f32_e32 v27, v10, v29
	v_mul_f32_e32 v26, v26, v32
	v_mul_f32_e32 v27, v27, v33
	v_cvt_pk_fp8_f32 v28, v26, v27 op_sel:[0,0,1]
	global_store_dword v[38:39], v28, off offset:256
	global_store_dword v[46:47], v28, off offset:256
	v_lshl_add_u64 v[26:27], s[38:39], 0, v[8:9]
	v_add_co_u32_e32 v34, vcc, 0x200000, v26
	v_lshl_add_u64 v[30:31], v[22:23], 0, s[6:7]
	s_nop 0
	v_addc_co_u32_e32 v35, vcc, 0, v27, vcc
	v_add_co_u32_e32 v36, vcc, 0x2000, v30
	v_mov_b64_e32 v[26:27], v[104:105]
	v_mov_b64_e32 v[28:29], v[106:107]
	s_nop 0
	v_addc_co_u32_e32 v37, vcc, 0, v31, vcc
	v_mov_b64_e32 v[30:31], v[136:137]
	v_mov_b64_e32 v[32:33], v[138:139]
	s_add_u32 s6, s6, 0x800
	s_addc_u32 s7, s7, 0
	v_lshl_add_u64 v[8:9], v[8:9], 0, s[56:57]
	s_cmpk_eq_i32 s6, 0x2000
	v_mul_f32_e32 v11, v10, v26
	v_mul_f32_e32 v13, v10, v27
	v_mul_f32_e32 v26, v10, v28
	v_mul_f32_e32 v11, v11, v30
	v_mul_f32_e32 v13, v13, v31
	v_mov_b32_e32 v28, v3
	v_cvt_pk_fp8_f32 v28, v11, v13
	v_mul_f32_e32 v27, v10, v29
	v_mul_f32_e32 v26, v26, v32
	v_mul_f32_e32 v27, v27, v33
	v_cvt_pk_fp8_f32 v28, v26, v27 op_sel:[0,0,1]
	v_lshl_add_u64 v[26:27], s[38:39], 0, v[4:5]
	v_add_co_u32_e32 v38, vcc, s72, v26
	v_lshl_add_u64 v[4:5], v[4:5], 0, s[88:89]
	s_nop 0
	v_addc_co_u32_e32 v39, vcc, 0, v27, vcc
	v_lshl_add_u64 v[26:27], s[38:39], 0, v[6:7]
	v_add_co_u32_e32 v46, vcc, s72, v26
	global_store_dword v[38:39], v28, off
	s_nop 0
	v_addc_co_u32_e32 v47, vcc, 0, v27, vcc
	global_store_dword v[46:47], v28, off
	v_mov_b64_e32 v[26:27], v[108:109]
	v_mov_b64_e32 v[28:29], v[110:111]
	s_nop 0
	v_mov_b64_e32 v[30:31], v[140:141]
	v_mov_b64_e32 v[32:33], v[142:143]
	v_lshl_add_u64 v[6:7], v[6:7], 0, s[88:89]
	v_mul_f32_e32 v11, v10, v26
	v_mul_f32_e32 v13, v10, v27
	v_mul_f32_e32 v11, v11, v30
	v_mul_f32_e32 v13, v13, v31
	v_mul_f32_e32 v26, v10, v28
	v_mov_b32_e32 v28, v3
	v_cvt_pk_fp8_f32 v28, v11, v13
	v_mul_f32_e32 v27, v10, v29
	v_mul_f32_e32 v26, v26, v32
	v_mul_f32_e32 v27, v27, v33
	v_cvt_pk_fp8_f32 v28, v26, v27 op_sel:[0,0,1]
	global_store_dword v[38:39], v28, off offset:256
	global_store_dword v[46:47], v28, off offset:256
	v_lshl_add_u64 v[26:27], s[38:39], 0, v[8:9]
	v_add_co_u32_e32 v34, vcc, 0x200000, v26
	v_lshl_add_u64 v[30:31], v[22:23], 0, s[6:7]
	s_nop 0
	v_addc_co_u32_e32 v35, vcc, 0, v27, vcc
	v_add_co_u32_e32 v36, vcc, 0x2000, v30
	v_mov_b64_e32 v[26:27], v[112:113]
	v_mov_b64_e32 v[28:29], v[114:115]
	s_nop 0
	v_addc_co_u32_e32 v37, vcc, 0, v31, vcc
	v_mov_b64_e32 v[30:31], v[144:145]
	v_mov_b64_e32 v[32:33], v[146:147]
	s_add_u32 s6, s6, 0x800
	s_addc_u32 s7, s7, 0
	v_lshl_add_u64 v[8:9], v[8:9], 0, s[56:57]
	s_cmpk_eq_i32 s6, 0x2000
	v_mul_f32_e32 v11, v10, v26
	v_mul_f32_e32 v13, v10, v27
	v_mul_f32_e32 v26, v10, v28
	v_mul_f32_e32 v11, v11, v30
	v_mul_f32_e32 v13, v13, v31
	v_mov_b32_e32 v28, v3
	v_cvt_pk_fp8_f32 v28, v11, v13
	v_mul_f32_e32 v27, v10, v29
	v_mul_f32_e32 v26, v26, v32
	v_mul_f32_e32 v27, v27, v33
	v_cvt_pk_fp8_f32 v28, v26, v27 op_sel:[0,0,1]
	v_lshl_add_u64 v[26:27], s[38:39], 0, v[4:5]
	v_add_co_u32_e32 v38, vcc, s72, v26
	v_lshl_add_u64 v[4:5], v[4:5], 0, s[88:89]
	s_nop 0
	v_addc_co_u32_e32 v39, vcc, 0, v27, vcc
	v_lshl_add_u64 v[26:27], s[38:39], 0, v[6:7]
	v_add_co_u32_e32 v46, vcc, s72, v26
	global_store_dword v[38:39], v28, off
	s_nop 0
	v_addc_co_u32_e32 v47, vcc, 0, v27, vcc
	global_store_dword v[46:47], v28, off
	v_mov_b64_e32 v[26:27], v[116:117]
	v_mov_b64_e32 v[28:29], v[118:119]
	s_nop 0
	v_mov_b64_e32 v[30:31], v[148:149]
	v_mov_b64_e32 v[32:33], v[150:151]
	v_lshl_add_u64 v[6:7], v[6:7], 0, s[88:89]
	v_mul_f32_e32 v11, v10, v26
	v_mul_f32_e32 v13, v10, v27
	v_mul_f32_e32 v11, v11, v30
	v_mul_f32_e32 v13, v13, v31
	v_mul_f32_e32 v26, v10, v28
	v_mov_b32_e32 v28, v3
	v_cvt_pk_fp8_f32 v28, v11, v13
	v_mul_f32_e32 v27, v10, v29
	v_mul_f32_e32 v26, v26, v32
	v_mul_f32_e32 v27, v27, v33
	v_cvt_pk_fp8_f32 v28, v26, v27 op_sel:[0,0,1]
	global_store_dword v[38:39], v28, off offset:256
	global_store_dword v[46:47], v28, off offset:256
	v_readlane_b32 s0, v254, 41
	v_readlane_b32 s6, v254, 35
	v_readlane_b32 s7, v254, 36
	v_add_u32_e32 v12, s0, v12
	s_movk_i32 s0, 0x1fff
	v_cmp_lt_i32_e32 vcc, s0, v12
	v_lshl_add_u64 v[20:21], v[20:21], 0, s[6:7]
	s_or_b64 s[14:15], vcc, s[14:15]
	v_lshl_add_u64 v[18:19], v[18:19], 0, s[6:7]
	v_readlane_b32 s1, v254, 42
	s_andn2_b64 exec, exec, s[14:15]
	s_cbranch_execnz .LBB6_1829
